# attention P.V: the first 32-column group's V-fragment LDS reads hoisted above the softmax-finish VALU section (right after the last QK^T MFMA), first fragment pair through spare registers v242-247
# baseline (speedup 1.0000x reference)
; __device__ __forceinline__ unsigned sel_bit_mask(unsigned w, int b) { unsigned m; asm("v_bfe_i32 %0, %1, %2, 1" : "=v"(m) : "v"(w), "n"(b)); return m; }
; template <bool SEL>
; __device__ __forceinline__ void finishSM(f32x16& p0, f32x16& p1, float alpha, float& l_reg, bf16x8& pa0, bf16x8& pa1, bf16x8& pa2, bf16x8& pa3, unsigned selw) {
; #pragma unroll
;     for (int r = 0; r < 16; ++r) p1[r] = __builtin_amdgcn_exp2f(p1[r]);
;     if (SEL) {
; #pragma unroll
;         for (int r = 0; r < 16; ++r) p1[r] = __uint_as_float(__float_as_uint(p1[r]) & sel_bit_mask(selw, 16 + r));
;     }
;     float ps = 0;
; #pragma unroll
;     for (int r = 0; r < 16; ++r) ps += p0[r];
; #pragma unroll
;     for (int r = 0; r < 16; ++r) ps += p1[r];
;     { auto rr = __builtin_amdgcn_permlane32_swap(__float_as_uint(ps), __float_as_uint(ps), false, false);
;       ps = __uint_as_float(rr[0]) + __uint_as_float(rr[1]); }
;     l_reg = l_reg * alpha + ps;
;     ...
;     PK4(p0, 0, pa0); PK4(p0, 8, pa1); PK4(p1, 0, pa2); PK4(p1, 8, pa3);
;     ...
; }
; template <int KB, int QREG>
; __device__ __forceinline__ void qkt(f32x16& p0, f32x16& p1, const char* K_lds, int r32, int hi, const bf16x8* qr, const char* qlds) {
;     p0 = f32x16{}; p1 = f32x16{};
;     const char* kb[4];
; #pragma unroll
;     for (int dd = 0; dd < 4; ++dd) kb[dd] = K_lds + KB * SHM_K + KSWZ(r32, (dd * 16 + hi * 8) * 2);
; #pragma unroll
;     for (int d0 = 0; d0 < 8; ++d0) { const char* a = kb[d0 & 3] + (d0 >> 2) * 128;
;         bf16x8 b0 = *reinterpret_cast<const bf16x8*>(a);
;         bf16x8 b1 = *reinterpret_cast<const bf16x8*>(a + 32 * 256);
;         const bf16x8 qf = (d0 < QREG) ? qr[d0 < QREG ? d0 : 0] : *reinterpret_cast<const bf16x8*>(qlds + (d0 - QREG) * 1024);
;         p0 = __builtin_amdgcn_mfma_f32_32x32x16_bf16(b0, qf, p0, 0, 0, 0);
;         p1 = __builtin_amdgcn_mfma_f32_32x32x16_bf16(b1, qf, p1, 0, 0, 0); }
; }
; template <int VB>
; __device__ __forceinline__ void pv_tile(f32x16* o, int vb0, bf16x8 pa0, bf16x8 pa1, bf16x8 pa2, bf16x8 pa3) {
;     ...
;     PV_D0(0); PV_D0(1); PV_D0(2); PV_D0(3);
.LBB0_1812:
	ds_read_b128 v[2:5], v213 offset:49152
	ds_read_b128 v[250:253], v212 offset:49152
	ds_read_b128 v[6:9], v213 offset:49280
	v_add_f32_e32 v0, 0, v126
	v_add_f32_e32 v0, v127, v0
	v_add_f32_e32 v0, v124, v0
	s_waitcnt lgkmcnt(2)
	v_mfma_f32_32x32x16_bf16 v[96:111], v[2:5], v[164:167], 0
	ds_read_b128 v[2:5], v213 offset:57344
	ds_read_b128 v[10:13], v212 offset:49280
	v_add_f32_e32 v0, v125, v0
	v_add_f32_e32 v0, v122, v0
	v_add_f32_e32 v0, v123, v0
	v_add_f32_e32 v0, v120, v0
	v_add_f32_e32 v0, v121, v0
	v_add_f32_e32 v0, v118, v0
	s_waitcnt lgkmcnt(3)
	v_mfma_f32_32x32x16_bf16 v[96:111], v[250:253], v[160:163], v[96:111]
	ds_read_b128 v[250:253], v212 offset:57344
	ds_read_b128 v[128:131], v213 offset:57472
	v_add_f32_e32 v0, v119, v0
	v_add_f32_e32 v0, v116, v0
	v_add_f32_e32 v0, v117, v0
	v_add_f32_e32 v0, v114, v0
	v_add_f32_e32 v0, v115, v0
	v_add_f32_e32 v0, v112, v0
	s_waitcnt lgkmcnt(3)
	v_mfma_f32_32x32x16_bf16 v[80:95], v[2:5], v[164:167], 0
	ds_read_b128 v[2:5], v211 offset:49152
	ds_read_b128 v[132:135], v212 offset:57472
	v_add_f32_e32 v0, v113, v0
	s_waitcnt lgkmcnt(3)
	v_mfma_f32_32x32x16_bf16 v[80:95], v[250:253], v[160:163], v[80:95]
	ds_read_b128 v[250:253], v211 offset:57344
	ds_read_b128 v[136:139], v211 offset:49280
	s_waitcnt lgkmcnt(3)
	v_mfma_f32_32x32x16_bf16 v[96:111], v[2:5], v[156:159], v[96:111]
	ds_read_b128 v[2:5], v210 offset:49152
	ds_read_b128 v[140:143], v211 offset:57472
	s_waitcnt lgkmcnt(3)
	v_mfma_f32_32x32x16_bf16 v[80:95], v[250:253], v[156:159], v[80:95]
	ds_read_b128 v[250:253], v210 offset:57344
	ds_read_b128 v[220:223], v210 offset:49280
	s_waitcnt lgkmcnt(3)
	v_mfma_f32_32x32x16_bf16 v[96:111], v[2:5], v[152:155], v[96:111]
	ds_read_b128 v[224:227], v210 offset:57472
	s_waitcnt lgkmcnt(2)
	v_mfma_f32_32x32x16_bf16 v[80:95], v[250:253], v[152:155], v[80:95]
	v_mfma_f32_32x32x16_bf16 v[96:111], v[6:9], v[148:151], v[96:111]
	ds_read_b128 v[2:5], v208
	ds_read_b128 v[6:9], v208 offset:1024
	v_cvt_pk_bf16_f32 v126, v126, v127
	v_cvt_pk_bf16_f32 v127, v124, v125
	v_exp_f32_e32 v124, v172
	v_exp_f32_e32 v125, v173
	v_mfma_f32_32x32x16_bf16 v[80:95], v[128:131], v[148:151], v[80:95]
	v_cvt_pk_bf16_f32 v128, v122, v123
	v_exp_f32_e32 v122, v174
	v_exp_f32_e32 v123, v175
	v_exp_f32_e32 v129, v170
	v_exp_f32_e32 v130, v171
	v_exp_f32_e32 v131, v168
	v_permlane32_swap_b32_e32 v126, v128
	v_mfma_f32_32x32x16_bf16 v[96:111], v[10:13], v[144:147], v[96:111]
	v_exp_f32_e32 v10, v178
	v_exp_f32_e32 v11, v179
	v_exp_f32_e32 v12, v176
	v_exp_f32_e32 v13, v177
	v_mfma_f32_32x32x16_bf16 v[80:95], v[132:135], v[144:147], v[80:95]
	v_bfe_i32 v133, v195, 16, 1
	v_exp_f32_e32 v132, v169
	s_waitcnt lgkmcnt(1)
	v_mfma_f32_32x32x16_bf16 v[96:111], v[136:139], v[2:5], v[96:111]
	v_mfma_f32_32x32x16_bf16 v[80:95], v[140:143], v[2:5], v[80:95]
	v_exp_f32_e32 v2, v182
	v_exp_f32_e32 v3, v183
	v_exp_f32_e32 v4, v180
	v_exp_f32_e32 v5, v181
	v_and_b32_e32 v2, v133, v2
	v_bfe_i32 v133, v195, 17, 1
	v_add_f32_e32 v0, v0, v2
	v_and_b32_e32 v3, v133, v3
	v_bfe_i32 v133, v195, 18, 1
	v_add_f32_e32 v0, v0, v3
	v_and_b32_e32 v4, v133, v4
	v_bfe_i32 v133, v195, 19, 1
	v_add_f32_e32 v0, v0, v4
	v_and_b32_e32 v5, v133, v5
	v_bfe_i32 v133, v195, 20, 1
	v_add_f32_e32 v0, v0, v5
	v_and_b32_e32 v10, v133, v10
	v_bfe_i32 v133, v195, 21, 1
	v_add_f32_e32 v0, v0, v10
	v_and_b32_e32 v11, v133, v11
	v_bfe_i32 v133, v195, 22, 1
	v_add_f32_e32 v0, v0, v11
	v_and_b32_e32 v12, v133, v12
	v_bfe_i32 v133, v195, 23, 1
	v_add_f32_e32 v0, v0, v12
	v_and_b32_e32 v13, v133, v13
	v_bfe_i32 v133, v195, 24, 1
	v_add_f32_e32 v0, v0, v13
	v_and_b32_e32 v122, v133, v122
	v_bfe_i32 v133, v195, 25, 1
	v_add_f32_e32 v0, v0, v122
	v_and_b32_e32 v123, v133, v123
	v_bfe_i32 v133, v195, 26, 1
	v_add_f32_e32 v0, v0, v123
	v_and_b32_e32 v124, v133, v124
	v_bfe_i32 v133, v195, 27, 1
	s_waitcnt lgkmcnt(0)
	v_mfma_f32_32x32x16_bf16 v[96:111], v[220:223], v[6:9], v[96:111]
	v_and_b32_e32 v125, v133, v125
	v_bfe_i32 v133, v195, 28, 1
	v_add_f32_e32 v0, v0, v124
	v_and_b32_e32 v133, v133, v129
	v_add_f32_e32 v0, v0, v125
	v_bfe_i32 v129, v195, 29, 1
	v_add_f32_e32 v0, v0, v133
	v_mfma_f32_32x32x16_bf16 v[80:95], v[224:227], v[6:9], v[80:95]
	ds_read_b64_tr_b16 v[242:243], v206 offset:0
	ds_read_b64_tr_b16 v[244:245], v206 offset:0x800
	ds_read_b64_tr_b16 v[134:135], v206 offset:0x1000
	ds_read_b64_tr_b16 v[136:137], v206 offset:0x1800
	ds_read_b64_tr_b16 v[138:139], v206 offset:0x2000
	ds_read_b64_tr_b16 v[140:141], v206 offset:0x2800
	ds_read_b64_tr_b16 v[172:173], v206 offset:0x3000
	ds_read_b64_tr_b16 v[174:175], v206 offset:0x3800
	v_and_b32_e32 v130, v129, v130
	v_bfe_i32 v129, v195, 30, 1
	v_add_f32_e32 v0, v0, v130
	v_and_b32_e32 v131, v129, v131
	v_bfe_i32 v129, v195, 31, 1
	v_add_f32_e32 v0, v0, v131
	v_and_b32_e32 v132, v129, v132
	v_add_f32_e32 v189, v0, v132
	v_mov_b32_e32 v219, v189
	v_cvt_pk_bf16_f32 v129, v120, v121
	v_cvt_pk_bf16_f32 v118, v118, v119
	v_cvt_pk_bf16_f32 v119, v116, v117
	v_cvt_pk_bf16_f32 v120, v114, v115
	v_cvt_pk_bf16_f32 v121, v112, v113
	v_cvt_pk_bf16_f32 v112, v2, v3
	v_cvt_pk_bf16_f32 v113, v4, v5
	v_cvt_pk_bf16_f32 v114, v10, v11
	v_cvt_pk_bf16_f32 v115, v12, v13
	v_cvt_pk_bf16_f32 v122, v122, v123
	v_cvt_pk_bf16_f32 v123, v124, v125
	v_cvt_pk_bf16_f32 v124, v133, v130
	v_cvt_pk_bf16_f32 v125, v131, v132
	s_nop 1
	v_permlane32_swap_b32_e32 v189, v219
	v_permlane32_swap_b32_e32 v127, v129
	v_permlane32_swap_b32_e32 v118, v120
	v_permlane32_swap_b32_e32 v119, v121
	v_permlane32_swap_b32_e32 v112, v114
	v_permlane32_swap_b32_e32 v113, v115
	v_permlane32_swap_b32_e32 v122, v124
	v_permlane32_swap_b32_e32 v123, v125
	v_add_u32_e32 v4, 32, v196
	v_add_u32_e32 v0, -2, v194
	v_ashrrev_i32_e32 v197, 31, v196
	v_ashrrev_i32_e32 v5, 31, v4
	v_lshl_add_u64 v[2:3], v[0:1], 2, s[44:45]
	v_lshlrev_b64 v[10:11], 10, v[196:197]
	v_lshlrev_b64 v[12:13], 10, v[4:5]
	global_load_dword v217, v[2:3], off
	v_lshl_add_u64 v[2:3], v[14:15], 0, v[10:11]
	v_lshl_add_u64 v[6:7], v[14:15], 0, v[12:13]
	v_lshl_add_u64 v[10:11], v[192:193], 0, v[10:11]
	global_load_dwordx4 v[2:5], v[2:3], off
	s_nop 0
	global_load_dwordx4 v[6:9], v[6:7], off
	v_lshl_add_u64 v[116:117], v[192:193], 0, v[12:13]
	global_load_dwordx4 v[10:13], v[10:11], off
	s_nop 0
	global_load_dwordx4 v[168:171], v[116:117], off
	s_nop 0
	s_waitcnt lgkmcnt(6)
; template <int VB>
; __device__ __forceinline__ void pv_tile(f32x16* o, int vb0, bf16x8 pa0, bf16x8 pa1, bf16x8 pa2, bf16x8 pa3) {
;     ...
;     PV_D0(0); PV_D0(1); PV_D0(2); PV_D0(3);
	v_mfma_f32_32x32x16_bf16 v[64:79], v[126:129], v[242:245], v[64:79]
	ds_read_b64_tr_b16 v[130:131], v206 offset:0x200
	ds_read_b64_tr_b16 v[132:133], v206 offset:0xa00
	s_waitcnt lgkmcnt(6)
	v_mfma_f32_32x32x16_bf16 v[64:79], v[118:121], v[134:137], v[64:79]
	ds_read_b64_tr_b16 v[134:135], v206 offset:0x1200
	ds_read_b64_tr_b16 v[136:137], v206 offset:0x1a00
	s_waitcnt lgkmcnt(6)
	v_mfma_f32_32x32x16_bf16 v[64:79], v[112:115], v[138:141], v[64:79]
	ds_read_b64_tr_b16 v[138:139], v206 offset:0x2200
	ds_read_b64_tr_b16 v[140:141], v206 offset:0x2a00
	ds_read_b64_tr_b16 v[176:177], v206 offset:0x3200
	ds_read_b64_tr_b16 v[178:179], v206 offset:0x3a00
	s_waitcnt lgkmcnt(8)
	v_mfma_f32_32x32x16_bf16 v[64:79], v[122:125], v[172:175], v[64:79]
	s_waitcnt lgkmcnt(6)
	v_mfma_f32_32x32x16_bf16 v[48:63], v[126:129], v[130:133], v[48:63]
	ds_read_b64_tr_b16 v[130:131], v206 offset:0x400
	ds_read_b64_tr_b16 v[132:133], v206 offset:0xc00
	s_waitcnt lgkmcnt(6)
	v_mfma_f32_32x32x16_bf16 v[48:63], v[118:121], v[134:137], v[48:63]
	ds_read_b64_tr_b16 v[134:135], v206 offset:0x1400
	ds_read_b64_tr_b16 v[136:137], v206 offset:0x1c00
	s_waitcnt lgkmcnt(6)
	v_mfma_f32_32x32x16_bf16 v[48:63], v[112:115], v[138:141], v[48:63]
	ds_read_b64_tr_b16 v[138:139], v206 offset:0x2400
	ds_read_b64_tr_b16 v[140:141], v206 offset:0x2c00
	ds_read_b64_tr_b16 v[172:173], v206 offset:0x3400
	ds_read_b64_tr_b16 v[174:175], v206 offset:0x3c00
	s_waitcnt lgkmcnt(8)
	v_mfma_f32_32x32x16_bf16 v[48:63], v[122:125], v[176:179], v[48:63]
	s_waitcnt lgkmcnt(6)
	v_mfma_f32_32x32x16_bf16 v[32:47], v[126:129], v[130:133], v[32:47]
	ds_read_b64_tr_b16 v[130:131], v206 offset:0x600
	ds_read_b64_tr_b16 v[132:133], v206 offset:0xe00
	s_waitcnt lgkmcnt(6)
	v_mfma_f32_32x32x16_bf16 v[32:47], v[118:121], v[134:137], v[32:47]
	ds_read_b64_tr_b16 v[134:135], v206 offset:0x1600
	ds_read_b64_tr_b16 v[136:137], v206 offset:0x1e00
	s_waitcnt lgkmcnt(6)
	v_mfma_f32_32x32x16_bf16 v[32:47], v[112:115], v[138:141], v[32:47]
	ds_read_b64_tr_b16 v[138:139], v206 offset:0x2600
	ds_read_b64_tr_b16 v[140:141], v206 offset:0x2e00
	ds_read_b64_tr_b16 v[176:177], v206 offset:0x3600
	ds_read_b64_tr_b16 v[178:179], v206 offset:0x3e00
	s_waitcnt lgkmcnt(8)
	v_mfma_f32_32x32x16_bf16 v[32:47], v[122:125], v[172:175], v[32:47]
	s_waitcnt lgkmcnt(6)
	v_mfma_f32_32x32x16_bf16 v[16:31], v[126:129], v[130:133], v[16:31]
	v_max_f32_e32 v0, v97, v97
	s_waitcnt lgkmcnt(0)
	s_barrier
	s_waitcnt vmcnt(0)
	s_waitcnt vmcnt(4)
	v_bfe_i32 v116, v217, 8, 1
	v_bfe_i32 v117, v217, 10, 1
	v_mfma_f32_32x32x16_bf16 v[16:31], v[118:121], v[134:137], v[16:31]
	v_bfe_i32 v120, v217, 1, 1
	v_bfe_i32 v121, v217, 3, 1
	v_bfe_i32 v118, v217, 12, 1
	v_bfe_i32 v126, v217, 13, 1
	v_bfe_i32 v119, v217, 14, 1
	v_bfe_i32 v127, v217, 15, 1
	s_waitcnt vmcnt(3)
	ds_write_b128 v216, v[2:5]
	s_waitcnt vmcnt(2)
	ds_write_b128 v218, v[6:9]
	s_waitcnt vmcnt(1)
	ds_write_b128 v204, v[10:13] offset:32768
	s_waitcnt vmcnt(0)
	ds_write_b128 v204, v[168:171] offset:40960
	v_mfma_f32_32x32x16_bf16 v[16:31], v[112:115], v[138:141], v[16:31]
	v_max_f32_e32 v112, v96, v96
	v_max_f32_e32 v0, v112, v0
	v_max3_f32 v0, v0, v98, v99
	v_max3_f32 v0, v0, v100, v101
	v_max3_f32 v0, v0, v102, v103
	v_max3_f32 v0, v0, v104, v105
	v_max3_f32 v0, v0, v106, v107
	v_max3_f32 v0, v0, v108, v109
	v_max3_f32 v0, v0, v110, v111
	v_max3_f32 v0, v0, v80, v81
	v_max3_f32 v0, v0, v82, v83
	v_max3_f32 v0, v0, v84, v85
	v_max3_f32 v0, v0, v86, v87
	v_max3_f32 v0, v0, v88, v89
	v_max3_f32 v0, v0, v90, v91
	v_max3_f32 v0, v0, v92, v93
	v_max3_f32 v0, v0, v94, v95
	v_mov_b32_e32 v112, v0
	s_nop 1
	v_permlane32_swap_b32_e32 v0, v112
	v_max_f32_e32 v112, v112, v112
	v_max_f32_e32 v0, v0, v0
	v_max_f32_e32 v0, v0, v112
	v_sub_f32_e32 v112, v0, v184
	v_mul_f32_e32 v112, 0x3db504f3, v112
	v_cmp_ge_f32_e32 vcc, s5, v112
	v_max_f32_e32 v112, v184, v184
	v_max_f32_e32 v128, v112, v0
	v_mfma_f32_32x32x16_bf16 v[16:31], v[122:125], v[176:179], v[16:31]
	v_sub_f32_e32 v0, v184, v128
	v_mul_f32_e32 v0, 0x3e0293ee, v0
	v_exp_f32_e32 v0, v0
	s_cmp_eq_u64 vcc, exec
	s_cselect_b64 s[2:3], -1, 0
	v_bfe_i32 v112, v217, 0, 1
	v_cndmask_b32_e64 v0, v0, 1.0, s[2:3]
	v_cmp_gt_f32_e32 vcc, 1.0, v0
	v_bfe_i32 v113, v217, 2, 1
	v_bfe_i32 v114, v217, 4, 1
	v_bfe_i32 v122, v217, 5, 1
	v_bfe_i32 v115, v217, 6, 1
	v_bfe_i32 v123, v217, 7, 1
	v_bfe_i32 v124, v217, 9, 1
	v_bfe_i32 v125, v217, 11, 1
	s_cbranch_vccz .LBB0_1816
	s_and_saveexec_b64 s[48:49], s[0:1]
	ds_write_b32 v205, v0 offset:128
	s_or_b64 exec, exec, s[48:49]
	s_waitcnt lgkmcnt(0)
	v_add_u32_e32 v129, s66, v203
	ds_read_b128 v[130:133], v129 offset:224
	ds_read_b128 v[134:137], v129 offset:192
	ds_read_b128 v[138:141], v129 offset:160
	ds_read_b128 v[172:175], v129 offset:128
	s_waitcnt lgkmcnt(3)
	v_pk_mul_f32 v[76:77], v[76:77], v[130:131]
	s_waitcnt lgkmcnt(2)
	v_pk_mul_f32 v[72:73], v[72:73], v[134:135]
	s_waitcnt lgkmcnt(1)
	v_pk_mul_f32 v[68:69], v[68:69], v[138:139]
	v_pk_mul_f32 v[78:79], v[78:79], v[132:133]
	v_pk_mul_f32 v[74:75], v[74:75], v[136:137]
	v_pk_mul_f32 v[70:71], v[70:71], v[140:141]
	s_waitcnt lgkmcnt(0)
	v_pk_mul_f32 v[66:67], v[66:67], v[174:175]
	v_pk_mul_f32 v[64:65], v[64:65], v[172:173]
	v_pk_mul_f32 v[60:61], v[60:61], v[130:131]
	v_pk_mul_f32 v[56:57], v[56:57], v[134:135]
	v_pk_mul_f32 v[52:53], v[52:53], v[138:139]
	v_pk_mul_f32 v[62:63], v[62:63], v[132:133]
	v_pk_mul_f32 v[58:59], v[58:59], v[136:137]
	v_pk_mul_f32 v[54:55], v[54:55], v[140:141]
	v_pk_mul_f32 v[50:51], v[50:51], v[174:175]
	v_pk_mul_f32 v[48:49], v[48:49], v[172:173]
	v_pk_mul_f32 v[44:45], v[44:45], v[130:131]
	v_pk_mul_f32 v[40:41], v[40:41], v[134:135]
	v_pk_mul_f32 v[36:37], v[36:37], v[138:139]
	v_pk_mul_f32 v[46:47], v[46:47], v[132:133]
	v_pk_mul_f32 v[42:43], v[42:43], v[136:137]
	v_pk_mul_f32 v[38:39], v[38:39], v[140:141]
	v_pk_mul_f32 v[34:35], v[34:35], v[174:175]
	v_pk_mul_f32 v[32:33], v[32:33], v[172:173]
	v_pk_mul_f32 v[28:29], v[28:29], v[130:131]
	v_pk_mul_f32 v[24:25], v[24:25], v[134:135]
	v_pk_mul_f32 v[20:21], v[20:21], v[138:139]
	v_pk_mul_f32 v[30:31], v[30:31], v[132:133]
	v_pk_mul_f32 v[26:27], v[26:27], v[136:137]
	v_pk_mul_f32 v[22:23], v[22:23], v[140:141]
	v_pk_mul_f32 v[18:19], v[18:19], v[174:175]
	v_pk_mul_f32 v[16:17], v[16:17], v[172:173]
; __device__ __forceinline__ unsigned sel_bit_mask(unsigned w, int b) { unsigned m; asm("v_bfe_i32 %0, %1, %2, 1" : "=v"(m) : "v"(w), "n"(b)); return m; }
; template <bool SEL>
; __device__ __forceinline__ void partialSM(f32x16& p0, f32x16& p1, float& m_reg, float& mn, float& alpha, unsigned selw) {
;     float pmax = p0[0];
; #pragma unroll
;     for (int r = 1; r < 16; ++r) pmax = fmaxf(pmax, p0[r]);
; #pragma unroll
;     for (int r = 0; r < 16; ++r) pmax = fmaxf(pmax, p1[r]);
;     { auto rr = __builtin_amdgcn_permlane32_swap(__float_as_uint(pmax), __float_as_uint(pmax), false, false);
;       pmax = fmaxf(__uint_as_float(rr[0]), __uint_as_float(rr[1])); }
;     constexpr float C2 = 1.4426950408889634f * SCALE;
;     if (__builtin_expect(__all((pmax - m_reg) * SCALE <= THR), 1)) { mn = m_reg; alpha = 1.f; }
;     else { mn = fmaxf(m_reg, pmax); alpha = __builtin_amdgcn_exp2f((m_reg - mn) * C2); m_reg = mn; }
;     const float mnL = -mn * C2;
; #pragma unroll
;     for (int r = 0; r < 16; ++r) p0[r] = fmaf(p0[r], C2, mnL);
; #pragma unroll
;     for (int r = 0; r < 16; ++r) p1[r] = fmaf(p1[r], C2, mnL);
; #pragma unroll
;     for (int r = 0; r < 16; ++r) p0[r] = __builtin_amdgcn_exp2f(p0[r]);
;     if (SEL) {
; #pragma unroll
;         for (int r = 0; r < 16; ++r) p0[r] = __uint_as_float(__float_as_uint(p0[r]) & sel_bit_mask(selw, r));
;     }
; template <int KB, int QREG>
; __device__ __forceinline__ void qkt(f32x16& p0, f32x16& p1, const char* K_lds, int r32, int hi, const bf16x8* qr, const char* qlds) {
;     p0 = f32x16{}; p1 = f32x16{};
;     const char* kb[4];
; #pragma unroll
;     for (int dd = 0; dd < 4; ++dd) kb[dd] = K_lds + KB * SHM_K + KSWZ(r32, (dd * 16 + hi * 8) * 2);
; #pragma unroll
;     for (int d0 = 0; d0 < 8; ++d0) { const char* a = kb[d0 & 3] + (d0 >> 2) * 128;
;         bf16x8 b0 = *reinterpret_cast<const bf16x8*>(a);
;         bf16x8 b1 = *reinterpret_cast<const bf16x8*>(a + 32 * 256);
;         const bf16x8 qf = (d0 < QREG) ? qr[d0 < QREG ? d0 : 0] : *reinterpret_cast<const bf16x8*>(qlds + (d0 - QREG) * 1024);
;         p0 = __builtin_amdgcn_mfma_f32_32x32x16_bf16(b0, qf, p0, 0, 0, 0);
;         p1 = __builtin_amdgcn_mfma_f32_32x32x16_bf16(b1, qf, p1, 0, 0, 0); }
; }
.LBB0_1816:
	v_cndmask_b32_e64 v197, v128, v184, s[2:3]
	v_mul_f32_e32 v172, 0xbe0293ee, v197
	v_fmamk_f32 v128, v96, 0x3e0293ee, v172
	v_fmamk_f32 v129, v97, 0x3e0293ee, v172
	v_fmamk_f32 v130, v98, 0x3e0293ee, v172
	v_fmamk_f32 v131, v99, 0x3e0293ee, v172
	v_fmamk_f32 v132, v100, 0x3e0293ee, v172
	v_fmamk_f32 v133, v101, 0x3e0293ee, v172
	v_fmamk_f32 v134, v102, 0x3e0293ee, v172
	v_fmamk_f32 v135, v103, 0x3e0293ee, v172
	v_fmamk_f32 v136, v104, 0x3e0293ee, v172
	v_fmamk_f32 v137, v105, 0x3e0293ee, v172
	v_fmamk_f32 v138, v106, 0x3e0293ee, v172
	v_fmamk_f32 v139, v107, 0x3e0293ee, v172
	v_fmamk_f32 v140, v108, 0x3e0293ee, v172
	v_fmamk_f32 v109, v109, 0x3e0293ee, v172
	v_fmamk_f32 v110, v110, 0x3e0293ee, v172
	v_fmamk_f32 v141, v111, 0x3e0293ee, v172
	v_fmamk_f32 v107, v80, 0x3e0293ee, v172
	v_fmamk_f32 v108, v81, 0x3e0293ee, v172
	v_fmamk_f32 v100, v82, 0x3e0293ee, v172
	v_fmamk_f32 v101, v83, 0x3e0293ee, v172
	v_fmamk_f32 v102, v84, 0x3e0293ee, v172
	v_fmamk_f32 v103, v85, 0x3e0293ee, v172
	v_fmamk_f32 v104, v86, 0x3e0293ee, v172
	v_fmamk_f32 v105, v87, 0x3e0293ee, v172
	v_fmamk_f32 v106, v88, 0x3e0293ee, v172
	v_fmamk_f32 v96, v89, 0x3e0293ee, v172
	v_fmamk_f32 v97, v90, 0x3e0293ee, v172
	v_fmamk_f32 v98, v91, 0x3e0293ee, v172
	v_fmamk_f32 v99, v92, 0x3e0293ee, v172
	v_exp_f32_e32 v80, v128
	v_exp_f32_e32 v81, v129
	v_exp_f32_e32 v82, v130
	v_exp_f32_e32 v83, v131
	v_exp_f32_e32 v84, v132
	v_exp_f32_e32 v85, v133
	v_exp_f32_e32 v86, v134
	v_exp_f32_e32 v87, v135
	v_exp_f32_e32 v88, v136
	v_exp_f32_e32 v89, v137
	v_exp_f32_e32 v90, v138
	v_exp_f32_e32 v91, v139
	v_exp_f32_e32 v92, v140
	v_exp_f32_e32 v128, v109
	v_exp_f32_e32 v111, v110
	v_exp_f32_e32 v129, v141
	v_fmamk_f32 v109, v93, 0x3e0293ee, v172
	v_fmamk_f32 v110, v94, 0x3e0293ee, v172
	v_fmac_f32_e32 v172, 0x3e0293ee, v95
	v_and_b32_e32 v81, v120, v81
	v_and_b32_e32 v80, v112, v80
	v_and_b32_e32 v83, v121, v83
	v_and_b32_e32 v82, v113, v82
	v_and_b32_e32 v85, v122, v85
	v_and_b32_e32 v84, v114, v84
	v_and_b32_e32 v87, v123, v87
	v_and_b32_e32 v86, v115, v86
	v_and_b32_e32 v89, v124, v89
	v_and_b32_e32 v88, v116, v88
	v_and_b32_e32 v91, v125, v91
	v_and_b32_e32 v90, v117, v90
	v_and_b32_e32 v93, v126, v128
	v_and_b32_e32 v92, v118, v92
	v_and_b32_e32 v95, v127, v129
	v_and_b32_e32 v94, v119, v111
	s_waitcnt lgkmcnt(0)
	s_barrier
	ds_read_b128 v[242:245], v208
	ds_read_b128 v[182:185], v208 offset:1024
	ds_read_b128 v[112:115], v213 offset:32768
	ds_read_b128 v[116:119], v213 offset:40960
	ds_read_b128 v[174:177], v212 offset:32768
	ds_read_b128 v[178:181], v212 offset:40960
	ds_read_b128 v[250:253], v211 offset:32768
	v_exp_f32_e32 v101, v101
	v_exp_f32_e32 v103, v103
	s_waitcnt lgkmcnt(4)
	v_mfma_f32_32x32x16_bf16 v[128:143], v[112:115], v[164:167], 0
	v_exp_f32_e32 v105, v105
	v_exp_f32_e32 v111, v96
	v_exp_f32_e32 v109, v109
	v_exp_f32_e32 v172, v172
	v_exp_f32_e32 v107, v107
	v_exp_f32_e32 v108, v108
	v_exp_f32_e32 v100, v100
	s_waitcnt lgkmcnt(3)
	v_mfma_f32_32x32x16_bf16 v[112:127], v[116:119], v[164:167], 0
	v_bfe_i32 v96, v217, 16, 1
	v_exp_f32_e32 v102, v102
	v_exp_f32_e32 v173, v97
	v_bfe_i32 v97, v217, 17, 1
	v_and_b32_e32 v96, v96, v107
	v_and_b32_e32 v97, v97, v108
	v_exp_f32_e32 v104, v104
	s_waitcnt lgkmcnt(2)
	v_mfma_f32_32x32x16_bf16 v[128:143], v[174:177], v[160:163], v[128:143]
	ds_read_b128 v[174:177], v211 offset:40960
	v_exp_f32_e32 v106, v106
	v_exp_f32_e32 v110, v110
	v_bfe_i32 v107, v217, 27, 1
	v_bfe_i32 v108, v217, 28, 1
	s_waitcnt lgkmcnt(2)
	v_mfma_f32_32x32x16_bf16 v[112:127], v[178:181], v[160:163], v[112:127]
	ds_read_b128 v[178:181], v210 offset:32768
	s_waitcnt lgkmcnt(2)
	v_mfma_f32_32x32x16_bf16 v[128:143], v[250:253], v[156:159], v[128:143]
	ds_read_b128 v[250:253], v210 offset:40960
	s_waitcnt lgkmcnt(2)
	v_mfma_f32_32x32x16_bf16 v[112:127], v[174:177], v[156:159], v[112:127]
	ds_read_b128 v[174:177], v213 offset:32896
	s_waitcnt lgkmcnt(2)
	v_mfma_f32_32x32x16_bf16 v[128:143], v[178:181], v[152:155], v[128:143]
	ds_read_b128 v[178:181], v213 offset:41088
	s_waitcnt lgkmcnt(2)
	v_mfma_f32_32x32x16_bf16 v[112:127], v[250:253], v[152:155], v[112:127]
	ds_read_b128 v[250:253], v212 offset:32896
	s_waitcnt lgkmcnt(2)
	v_mfma_f32_32x32x16_bf16 v[128:143], v[174:177], v[148:151], v[128:143]
	ds_read_b128 v[174:177], v212 offset:41088
	s_waitcnt lgkmcnt(2)
	v_mfma_f32_32x32x16_bf16 v[112:127], v[178:181], v[148:151], v[112:127]
	ds_read_b128 v[178:181], v211 offset:32896
	s_waitcnt lgkmcnt(2)
	v_mfma_f32_32x32x16_bf16 v[128:143], v[250:253], v[144:147], v[128:143]
	ds_read_b128 v[250:253], v211 offset:41088
	s_waitcnt lgkmcnt(2)
	v_mfma_f32_32x32x16_bf16 v[112:127], v[174:177], v[144:147], v[112:127]
	ds_read_b128 v[174:177], v210 offset:32896
	s_waitcnt lgkmcnt(2)
	v_mfma_f32_32x32x16_bf16 v[128:143], v[178:181], v[242:245], v[128:143]
	ds_read_b128 v[178:181], v210 offset:41088
	s_waitcnt lgkmcnt(2)
	v_mfma_f32_32x32x16_bf16 v[112:127], v[250:253], v[242:245], v[112:127]
	s_waitcnt lgkmcnt(1)
	v_mfma_f32_32x32x16_bf16 v[128:143], v[174:177], v[182:185], v[128:143]
	v_exp_f32_e32 v175, v99
	v_bfe_i32 v99, v217, 19, 1
	v_exp_f32_e32 v174, v98
	v_and_b32_e32 v99, v99, v101
	v_bfe_i32 v101, v217, 21, 1
	v_bfe_i32 v98, v217, 18, 1
	v_and_b32_e32 v107, v107, v174
	v_and_b32_e32 v101, v101, v103
	v_bfe_i32 v103, v217, 23, 1
	v_and_b32_e32 v98, v98, v100
	v_and_b32_e32 v103, v103, v105
	v_bfe_i32 v105, v217, 25, 1
	v_bfe_i32 v100, v217, 20, 1
	s_waitcnt lgkmcnt(0)
; __device__ __forceinline__ unsigned sel_bit_mask(unsigned w, int b) { unsigned m; asm("v_bfe_i32 %0, %1, %2, 1" : "=v"(m) : "v"(w), "n"(b)); return m; }
; template <bool SEL>
; __device__ __forceinline__ void finishSM(f32x16& p0, f32x16& p1, float alpha, float& l_reg, bf16x8& pa0, bf16x8& pa1, bf16x8& pa2, bf16x8& pa3, unsigned selw) {
; #pragma unroll
;     for (int r = 0; r < 16; ++r) p1[r] = __builtin_amdgcn_exp2f(p1[r]);
;     if (SEL) {
; #pragma unroll
;         for (int r = 0; r < 16; ++r) p1[r] = __uint_as_float(__float_as_uint(p1[r]) & sel_bit_mask(selw, 16 + r));
;     }
;     float ps = 0;
; #pragma unroll
;     for (int r = 0; r < 16; ++r) ps += p0[r];
; #pragma unroll
;     for (int r = 0; r < 16; ++r) ps += p1[r];
;     { auto rr = __builtin_amdgcn_permlane32_swap(__float_as_uint(ps), __float_as_uint(ps), false, false);
;       ps = __uint_as_float(rr[0]) + __uint_as_float(rr[1]); }
;     l_reg = l_reg * alpha + ps;
;     ...
;     PK4(p0, 0, pa0); PK4(p0, 8, pa1); PK4(p1, 0, pa2); PK4(p1, 8, pa3);
;     ...
; }
	v_mfma_f32_32x32x16_bf16 v[112:127], v[178:181], v[182:185], v[112:127]
	ds_read_b64_tr_b16 v[244:245], v206 offset:0x4000
	ds_read_b64_tr_b16 v[246:247], v206 offset:0x4800
	ds_read_b64_tr_b16 v[226:227], v206 offset:0x5000
	ds_read_b64_tr_b16 v[228:229], v206 offset:0x5800
	ds_read_b64_tr_b16 v[230:231], v206 offset:0x6000
	ds_read_b64_tr_b16 v[232:233], v206 offset:0x6800
	ds_read_b64_tr_b16 v[234:235], v206 offset:0x7000
	ds_read_b64_tr_b16 v[236:237], v206 offset:0x7800
	v_and_b32_e32 v105, v105, v111
	v_bfe_i32 v111, v217, 29, 1
	v_and_b32_e32 v100, v100, v102
	v_and_b32_e32 v109, v111, v109
	v_bfe_i32 v111, v217, 31, 1
	v_bfe_i32 v102, v217, 22, 1
	v_and_b32_e32 v108, v108, v175
	v_and_b32_e32 v111, v111, v172
	v_add_f32_e32 v172, 0, v80
	v_add_f32_e32 v172, v172, v81
	v_add_f32_e32 v172, v172, v82
	v_add_f32_e32 v172, v172, v83
	v_add_f32_e32 v172, v172, v84
	v_add_f32_e32 v172, v172, v85
	v_add_f32_e32 v172, v172, v86
	v_add_f32_e32 v172, v172, v87
	v_add_f32_e32 v172, v172, v88
	v_add_f32_e32 v172, v172, v89
	v_add_f32_e32 v172, v172, v90
	v_add_f32_e32 v172, v172, v91
	v_add_f32_e32 v172, v172, v92
	v_add_f32_e32 v172, v172, v93
	v_add_f32_e32 v172, v172, v94
	v_add_f32_e32 v172, v172, v95
	v_add_f32_e32 v172, v172, v96
	v_add_f32_e32 v172, v172, v97
	v_add_f32_e32 v172, v172, v98
	v_add_f32_e32 v172, v172, v99
	v_add_f32_e32 v172, v172, v100
	v_and_b32_e32 v102, v102, v104
	v_add_f32_e32 v172, v172, v101
	v_bfe_i32 v104, v217, 24, 1
	v_add_f32_e32 v172, v172, v102
	v_and_b32_e32 v104, v104, v106
	v_add_f32_e32 v172, v172, v103
	v_bfe_i32 v106, v217, 26, 1
	v_add_f32_e32 v172, v172, v104
	v_and_b32_e32 v106, v106, v173
	v_add_f32_e32 v172, v172, v105
	v_add_f32_e32 v172, v172, v106
	v_add_f32_e32 v172, v172, v107
	v_add_f32_e32 v172, v172, v108
	v_bfe_i32 v173, v217, 30, 1
	v_add_f32_e32 v172, v172, v109
	v_and_b32_e32 v110, v173, v110
	v_add_f32_e32 v172, v172, v110
	v_add_f32_e32 v220, v172, v111
	v_mov_b32_e32 v221, v220
	v_cvt_pk_bf16_f32 v172, v80, v81
	v_cvt_pk_bf16_f32 v173, v82, v83
	v_cvt_pk_bf16_f32 v174, v84, v85
	v_cvt_pk_bf16_f32 v175, v86, v87
	v_cvt_pk_bf16_f32 v176, v88, v89
	v_cvt_pk_bf16_f32 v177, v90, v91
	v_cvt_pk_bf16_f32 v178, v92, v93
	v_cvt_pk_bf16_f32 v179, v94, v95
	v_cvt_pk_bf16_f32 v180, v96, v97
	v_cvt_pk_bf16_f32 v181, v98, v99
	v_cvt_pk_bf16_f32 v182, v100, v101
	v_cvt_pk_bf16_f32 v183, v102, v103
	v_cvt_pk_bf16_f32 v184, v104, v105
	v_cvt_pk_bf16_f32 v185, v106, v107
	v_cvt_pk_bf16_f32 v186, v108, v109
	v_cvt_pk_bf16_f32 v187, v110, v111
	s_nop 1
	v_permlane32_swap_b32_e32 v220, v221
	v_permlane32_swap_b32_e32 v172, v174
	v_permlane32_swap_b32_e32 v173, v175
	v_permlane32_swap_b32_e32 v176, v178
	v_permlane32_swap_b32_e32 v177, v179
	v_permlane32_swap_b32_e32 v180, v182
	v_permlane32_swap_b32_e32 v181, v183
	v_permlane32_swap_b32_e32 v184, v186
	v_permlane32_swap_b32_e32 v185, v187
	v_mov_b32_e32 v195, v1
	v_lshl_add_u64 v[222:223], v[194:195], 2, s[44:45]
	global_load_dword v195, v[222:223], off
	s_add_i32 s2, s54, 1
	s_cmp_lt_i32 s2, s87
	s_cselect_b64 s[48:49], -1, 0
	s_cmp_ge_i32 s2, s87
	s_cbranch_scc1 .LBB0_1818
	v_add_u32_e32 v2, 64, v196
	v_add_u32_e32 v4, 0x60, v196
	v_ashrrev_i32_e32 v3, 31, v2
	v_ashrrev_i32_e32 v5, 31, v4
	v_lshlrev_b64 v[10:11], 10, v[2:3]
	v_lshlrev_b64 v[12:13], 10, v[4:5]
	v_lshl_add_u64 v[2:3], v[14:15], 0, v[10:11]
	v_lshl_add_u64 v[6:7], v[14:15], 0, v[12:13]
	v_lshl_add_u64 v[10:11], v[192:193], 0, v[10:11]
	v_lshl_add_u64 v[168:169], v[192:193], 0, v[12:13]
	global_load_dwordx4 v[2:5], v[2:3], off
	s_nop 0
	global_load_dwordx4 v[6:9], v[6:7], off
	s_nop 0
	global_load_dwordx4 v[10:13], v[10:11], off
	s_nop 0
	global_load_dwordx4 v[168:171], v[168:169], off
; template <int VB>
; __device__ __forceinline__ void pv_tile(f32x16* o, int vb0, bf16x8 pa0, bf16x8 pa1, bf16x8 pa2, bf16x8 pa3) {
;     ...
;     PV_D0(0); PV_D0(1); PV_D0(2); PV_D0(3);
.LBB0_1818:
	s_nop 0
	s_waitcnt lgkmcnt(6)
	v_mfma_f32_32x32x16_bf16 v[64:79], v[172:175], v[244:247], v[64:79]
	ds_read_b64_tr_b16 v[222:223], v206 offset:0x4200
	ds_read_b64_tr_b16 v[224:225], v206 offset:0x4a00
	s_waitcnt lgkmcnt(6)
	v_mfma_f32_32x32x16_bf16 v[64:79], v[176:179], v[226:229], v[64:79]
	ds_read_b64_tr_b16 v[226:227], v206 offset:0x5200
	ds_read_b64_tr_b16 v[228:229], v206 offset:0x5a00
	s_waitcnt lgkmcnt(6)
	v_mfma_f32_32x32x16_bf16 v[64:79], v[180:183], v[230:233], v[64:79]
	ds_read_b64_tr_b16 v[230:231], v206 offset:0x6200
	ds_read_b64_tr_b16 v[232:233], v206 offset:0x6a00
	ds_read_b64_tr_b16 v[238:239], v206 offset:0x7200
	ds_read_b64_tr_b16 v[240:241], v206 offset:0x7a00
	s_waitcnt lgkmcnt(8)
	v_mfma_f32_32x32x16_bf16 v[64:79], v[184:187], v[234:237], v[64:79]
	s_waitcnt lgkmcnt(6)
	v_mfma_f32_32x32x16_bf16 v[48:63], v[172:175], v[222:225], v[48:63]
	ds_read_b64_tr_b16 v[222:223], v206 offset:0x4400
	ds_read_b64_tr_b16 v[224:225], v206 offset:0x4c00
	s_waitcnt lgkmcnt(6)
	v_mfma_f32_32x32x16_bf16 v[48:63], v[176:179], v[226:229], v[48:63]
	ds_read_b64_tr_b16 v[226:227], v206 offset:0x5400
	ds_read_b64_tr_b16 v[228:229], v206 offset:0x5c00
	s_waitcnt lgkmcnt(6)
	v_mfma_f32_32x32x16_bf16 v[48:63], v[180:183], v[230:233], v[48:63]
	ds_read_b64_tr_b16 v[230:231], v206 offset:0x6400
	ds_read_b64_tr_b16 v[232:233], v206 offset:0x6c00
	ds_read_b64_tr_b16 v[234:235], v206 offset:0x7400
	ds_read_b64_tr_b16 v[236:237], v206 offset:0x7c00
	s_waitcnt lgkmcnt(8)
	v_mfma_f32_32x32x16_bf16 v[48:63], v[184:187], v[238:241], v[48:63]
	s_waitcnt lgkmcnt(6)
	v_mfma_f32_32x32x16_bf16 v[32:47], v[172:175], v[222:225], v[32:47]
	ds_read_b64_tr_b16 v[222:223], v206 offset:0x4600
	ds_read_b64_tr_b16 v[224:225], v206 offset:0x4e00
	s_waitcnt lgkmcnt(6)
	v_mfma_f32_32x32x16_bf16 v[32:47], v[176:179], v[226:229], v[32:47]
	ds_read_b64_tr_b16 v[226:227], v206 offset:0x5600
	ds_read_b64_tr_b16 v[228:229], v206 offset:0x5e00
	s_waitcnt lgkmcnt(6)
	v_mfma_f32_32x32x16_bf16 v[32:47], v[180:183], v[230:233], v[32:47]
	ds_read_b64_tr_b16 v[230:231], v206 offset:0x6600
	ds_read_b64_tr_b16 v[232:233], v206 offset:0x6e00
	ds_read_b64_tr_b16 v[238:239], v206 offset:0x7600
	ds_read_b64_tr_b16 v[240:241], v206 offset:0x7e00
	s_waitcnt lgkmcnt(8)
	v_mfma_f32_32x32x16_bf16 v[32:47], v[184:187], v[234:237], v[32:47]
	s_waitcnt lgkmcnt(6)
	v_mfma_f32_32x32x16_bf16 v[16:31], v[172:175], v[222:225], v[16:31]
	v_max_f32_e32 v172, v129, v129
	v_max_f32_e32 v173, v128, v128
	v_max_f32_e32 v172, v173, v172
	v_max3_f32 v172, v172, v130, v131
	v_max3_f32 v172, v172, v132, v133
	v_max3_f32 v172, v172, v134, v135
	v_max3_f32 v172, v172, v136, v137
	s_waitcnt lgkmcnt(4)
	v_mfma_f32_32x32x16_bf16 v[16:31], v[176:179], v[226:229], v[16:31]
	v_max3_f32 v172, v172, v138, v139
	v_max3_f32 v172, v172, v140, v141
	v_max3_f32 v172, v172, v142, v143
	v_max3_f32 v172, v172, v112, v113
	v_max3_f32 v172, v172, v114, v115
	v_max3_f32 v172, v172, v116, v117
	v_max3_f32 v172, v172, v118, v119
	s_waitcnt lgkmcnt(2)
	v_mfma_f32_32x32x16_bf16 v[16:31], v[180:183], v[230:233], v[16:31]
	v_max3_f32 v172, v172, v120, v121
	v_max3_f32 v172, v172, v122, v123
	v_max3_f32 v172, v172, v124, v125
	v_max3_f32 v172, v172, v126, v127
	v_mov_b32_e32 v173, v172
	s_nop 1
	v_permlane32_swap_b32_e32 v172, v173
	s_waitcnt lgkmcnt(0)
	v_mfma_f32_32x32x16_bf16 v[16:31], v[184:187], v[238:241], v[16:31]
	v_max_f32_e32 v173, v173, v173
	v_max_f32_e32 v172, v172, v172
	v_max_f32_e32 v172, v172, v173
	v_sub_f32_e32 v173, v172, v197
	v_mul_f32_e32 v173, 0x3db504f3, v173
	v_cmp_ge_f32_e32 vcc, s5, v173
	s_cmp_eq_u64 vcc, exec
	s_cselect_b64 s[2:3], -1, 0
	s_andn2_b64 vcc, exec, s[48:49]
	s_waitcnt vmcnt(0)
	v_bfe_i32 v185, v195, 0, 1
	v_bfe_i32 v186, v195, 1, 1
	v_bfe_i32 v187, v195, 2, 1
	v_bfe_i32 v222, v195, 3, 1
	v_bfe_i32 v223, v195, 4, 1
	v_bfe_i32 v224, v195, 5, 1
	v_bfe_i32 v225, v195, 6, 1
	v_bfe_i32 v226, v195, 7, 1
	v_bfe_i32 v227, v195, 8, 1
	v_bfe_i32 v228, v195, 9, 1
	v_bfe_i32 v229, v195, 10, 1
	v_bfe_i32 v230, v195, 11, 1
	v_bfe_i32 v231, v195, 12, 1
	v_bfe_i32 v232, v195, 13, 1
	v_bfe_i32 v233, v195, 14, 1
	v_bfe_i32 v234, v195, 15, 1
	s_barrier
	s_cbranch_vccnz .LBB0_1820
	s_waitcnt vmcnt(0)
	ds_write_b128 v216, v[2:5] offset:16384
	ds_write_b128 v218, v[6:9] offset:16384
	ds_write_b128 v204, v[10:13] offset:49152
	ds_write_b128 v204, v[168:171] offset:57344
